# in-proj GEMM main loop: LDS-DMA staging (global_load_lds_dwordx4 straight into the swizzled LDS image of the other stage, no staging registers, no ds_write); B image repacked without row padding, 32-b
# speedup vs baseline: 1.0318x; 1.0090x over previous
;     const int lane = tid & 63, wid = tid >> 6, wr = wid >> 1, wc = wid & 1, fr = lane & 15, fq = lane >> 4;
; #pragma unroll
;     for (int m = 0; m < 4; ++m)
; #pragma unroll
;         for (int n = 0; n < 4; ++n) acc[m][n] = (f32x4){0.f, 0.f, 0.f, 0.f};
;     unsigned ao[4];
; #pragma unroll
;     for (int i = 0; i < 4; ++i) ao[i] = arow((tid >> 3) + 32 * i) + (tid & 7) * 8;
;     const int bk = tid >> 4, bnc = tid & 15;
;     constexpr int NRB = B_F32 ? 8 : 4;
;     u32x4 ra0[4], ra1[4]; u32x4 rb0[NRB], rb1[NRB];
;     auto gloadA = [&](int kt, u32x4 (&ra)[4]) __attribute__((always_inline)) {
; #pragma unroll
;         for (int i = 0; i < 4; ++i) ra[i] = *(const u32x4*)(Abase + (ao[i] + kt * 64));
;     };
;     auto gloadB = [&](int kt, u32x4 (&rb)[NRB]) __attribute__((always_inline)) {
;         if (B_F32) {
;             const float* bp = (const float*)Bbase + (boff + (unsigned)((kt * 64 + bk) * ldb));
; #pragma unroll
;             for (int i = 0; i < 4; ++i) {
;                 if (bval) { rb[2 * i] = *(const u32x4*)(bp + (unsigned)(16 * i * ldb)); rb[2 * i + 1] = *(const u32x4*)(bp + (unsigned)(16 * i * ldb) + 4); }
;                 else { rb[2 * i] = (u32x4){0u, 0u, 0u, 0u}; rb[2 * i + 1] = rb[2 * i]; }
;             }
;         } else {
;             const bf16* bp = (const bf16*)Bbase + (boff + (unsigned)((kt * 64 + bk) * ldb));
; #pragma unroll
;             for (int i = 0; i < 4; ++i) rb[i] = bval ? *(const u32x4*)(bp + (unsigned)(16 * i * ldb)) : (u32x4){0u, 0u, 0u, 0u};
;         }
;     };
;     auto lstore = [&](const u32x4 (&ra)[4], const u32x4 (&rb)[NRB]) __attribute__((always_inline)) {
; #pragma unroll
;         for (int i = 0; i < 4; ++i) { const int row = (tid >> 3) + 32 * i, kc = tid & 7;
;             const u32x4 v = (kc & 1) ? (u32x4){ra[i][2], ra[i][3], ra[i][0], ra[i][1]} : ra[i];
; __device__ __forceinline__ void ph_inproj_mfma(const Ctx& c, int layer, int tile, unsigned char* lds) {
;     const int mt = tile / 18, nt = tile % 18;
;     const bf16* HA = c.w<bf16>(WS_HA) + (size_t)mt * 128 * D;
;     f32x4 acc[4][4];
;     const int vc = nt * 128 + (c.tid & 15) * 8;
;     gemm_tile<false, 1>(c.tid, lds, HA, [&](int r) __attribute__((always_inline)) { return (unsigned)(r * D); }, c.w<bf16>(WS_BIN) + (size_t)layer * D * DINV, (unsigned)vc, DINV, true, D, acc);
.LBB0_544:
	s_andn2_b64 vcc, exec, s[0:1]
	s_cbranch_vccnz .LBB0_533
	s_mul_hi_i32 s0, s60, 0x38e38e39
	s_load_dwordx2 s[42:43], s[4:5], 0x130
	s_lshr_b32 s1, s0, 31
	s_ashr_i32 s0, s0, 2
	s_add_i32 s28, s0, s1
	s_mul_i32 s0, s28, 18
	s_ashr_i32 s29, s28, 31
	s_sub_i32 s17, s60, s0
	s_lshl_b64 s[0:1], s[28:29], 18
	s_waitcnt lgkmcnt(0)
	s_add_u32 s0, s42, s0
	s_addc_u32 s1, s43, s1
	s_add_u32 s44, s0, 0x45c6000
	s_addc_u32 s45, s1, 0
	s_lshl_b32 s61, s17, 7
	s_add_u32 s0, s42, s59
	s_waitcnt vmcnt(0)
	v_lshlrev_b32_e32 v12, 3, v147
	s_addc_u32 s1, s43, s58
	s_add_u32 s46, s0, 0x18095100
	v_lshlrev_b32_e32 v2, 7, v147
	v_and_b32_e32 v4, 56, v12
	s_movk_i32 s0, 0xfc00
	v_and_b32_e32 v155, 15, v147
	v_and_or_b32 v2, v2, s0, v4
	v_lshrrev_b32_e32 v5, 1, v147
	s_mov_b32 s0, 0x3ffffc0
	v_bfe_u32 v157, v147, 4, 2
	v_and_or_b32 v5, v5, s0, v155
	v_bfe_u32 v7, v147, 4, 1
	v_lshlrev_b32_e32 v16, 6, v5
	v_lshlrev_b32_e32 v118, 3, v157
	v_bfe_u32 v5, v147, 2, 2
	v_lshlrev_b32_e32 v9, 2, v7
	v_or3_b32 v5, v9, v5, v118
	v_lshlrev_b32_e32 v9, 1, v147
	v_and_b32_e32 v9, 0x80, v9
	s_movk_i32 s7, 0x120
	v_mad_u32_u24 v5, v5, s7, v9
	v_and_b32_e32 v13, 0x78, v12
	v_add_u32_e32 v4, 0x8000, v2
	v_add_u32_e32 v6, 0x10000, v2
	v_ashrrev_i32_e32 v15, 4, v147
	v_and_or_b32 v119, v12, 24, v5
	v_cmp_eq_u32_e32 vcc, 0, v7
	v_mov_b32_e32 v5, v3
	v_mov_b32_e32 v7, v3
	s_movk_i32 s0, 0x900
	v_or_b32_e32 v14, s61, v13
	v_lshl_add_u64 v[4:5], v[4:5], 1, s[44:45]
	v_lshl_add_u64 v[6:7], v[6:7], 1, s[44:45]
	v_mul_lo_u32 v18, v15, s0
	s_addc_u32 s47, s1, 0
	v_add_u32_e32 v8, 0x18000, v2
	v_mov_b32_e32 v9, v3
	v_add_u32_e32 v6, v14, v18
	v_mov_b32_e32 v7, v3
	v_lshl_add_u64 v[4:5], v[8:9], 1, s[44:45]
	v_lshl_add_u64 v[6:7], v[6:7], 1, s[46:47]
	s_mov_b32 s0, 0x12000
	v_cndmask_b32_e32 v17, v236, v237, vcc
	v_add_co_u32_e32 v4, vcc, s0, v6
	s_mov_b32 s0, 0x24000
	s_nop 0
	v_addc_co_u32_e32 v5, vcc, 0, v7, vcc
	v_add_co_u32_e32 v8, vcc, s0, v6
	s_mov_b32 s0, 0x36000
	s_nop 0
	v_addc_co_u32_e32 v9, vcc, 0, v7, vcc
	v_add_co_u32_e32 v4, vcc, s0, v6
	v_lshl_add_u64 v[10:11], v[2:3], 1, s[44:45]
	s_nop 0
	v_addc_co_u32_e32 v5, vcc, 0, v7, vcc
	v_add_u32_e32 v6, 0x8040, v2
	v_mov_b32_e32 v7, v3
	v_lshl_add_u64 v[6:7], v[6:7], 1, s[44:45]
	v_add_u32_e32 v4, 0x10040, v2
	v_mov_b32_e32 v5, v3
	v_lshl_add_u64 v[4:5], v[4:5], 1, s[44:45]
	v_add_u32_e32 v6, 0x18040, v2
	v_mov_b32_e32 v7, v3
	v_lshl_add_u64 v[6:7], v[6:7], 1, s[44:45]
	v_and_b32_e32 v4, 1, v147
	v_cmp_eq_u32_e64 s[0:1], 0, v4
	v_bfe_i32 v4, v147, 2, 1
	v_and_b32_e32 v4, 0x2040, v4
	v_and_b32_e32 v5, 0xffffffc0, v12
	v_lshl_add_u32 v7, s60, 7, v18
	v_add_u32_e32 v4, v4, v5
	v_lshlrev_b32_e32 v5, 4, v147
	v_mul_lo_u32 v6, v15, s7
	v_or_b32_e32 v7, v7, v13
	s_mul_i32 s7, s28, 0x900
	v_lshlrev_b32_e32 v122, 4, v157
	v_and_b32_e32 v5, 48, v5
	v_lshlrev_b32_e32 v153, 4, v155
	v_subrev_u32_e32 v7, s7, v7
	v_mov_b32_e32 v20, 0
	v_lshrrev_b32_e32 v149, 4, v147
	s_mov_b32 s6, 0
	v_add_u32_e32 v116, 0x48000, v7
	v_add_u32_e32 v120, 0x10080, v2
	v_add_u32_e32 v123, v4, v5
	v_add_u32_e32 v124, v6, v153
	v_add_u32_e32 v125, v16, v122
	v_add_u32_e32 v126, v119, v17
	v_bfe_u32 v120, v147, 2, 2
	v_sub_u32_e32 v120, 0, v120
	v_and_b32_e32 v120, 3, v120
	v_lshlrev_b32_e32 v120, 4, v120
	v_xor_b32_e32 v216, v125, v120
	v_bfe_u32 v120, v147, 4, 2
	v_lshlrev_b32_e32 v120, 3, v120
	v_bfe_u32 v121, v147, 2, 2
	v_add_u32_e32 v120, v120, v121
	v_lshlrev_b32_e32 v120, 8, v120
	v_lshrrev_b32_e32 v68, 6, v147
	v_lshrrev_b32_e32 v214, 4, v147
	v_xor_b32_e32 v68, v68, v214
	v_and_b32_e32 v68, 1, v68
	v_lshlrev_b32_e32 v68, 7, v68
	v_or_b32_e32 v120, v120, v68
	v_and_b32_e32 v68, 3, v147
	v_lshlrev_b32_e32 v68, 3, v68
	v_or_b32_e32 v120, v120, v68
	v_xor_b32_e32 v68, 0, v121
	v_lshl_or_b32 v214, v68, 5, v120
	v_xor_b32_e32 v68, 1, v121
	v_lshl_or_b32 v215, v68, 5, v120
	v_xor_b32_e32 v68, 2, v121
	v_lshl_or_b32 v217, v68, 5, v120
	v_xor_b32_e32 v68, 3, v121
	v_lshl_or_b32 v218, v68, 5, v120
	v_lshrrev_b32_e32 v120, 6, v147
	s_nop 1
	v_readfirstlane_b32 s98, v120
	s_nop 1
	s_lshl_b32 s99, s98, 12
	s_lshl_b32 s98, s98, 11
	s_lshl_b32 s100, s61, 1
	v_lshrrev_b32_e32 v120, 6, v147
	v_lshlrev_b32_e32 v120, 5, v120
	v_bfe_u32 v121, v147, 2, 4
	v_add_u32_e32 v120, v120, v121
	v_mul_u32_u24_e32 v120, 0x800, v120
	v_bfe_u32 v121, v147, 4, 2
	v_sub_u32_e32 v121, 0, v121
	v_and_b32_e32 v121, 3, v121
	v_and_b32_e32 v68, 3, v147
	v_xor_b32_e32 v121, v121, v68
	v_lshl_add_u32 v206, v121, 4, v120
	v_add_u32_e32 v207, 64, v206
	v_add_u32_e32 v208, 0x8000, v206
	v_add_u32_e32 v209, 64, v208
	v_lshrrev_b32_e32 v120, 6, v147
	v_lshlrev_b32_e32 v120, 4, v120
	v_bfe_u32 v121, v147, 4, 2
	v_add_u32_e32 v120, v120, v121
	v_mul_u32_u24_e32 v120, 0x1200, v120
	v_add_u32_e32 v120, s100, v120
	v_bfe_u32 v68, v147, 1, 3
	v_xor_b32_e32 v68, v68, v121
	v_lshlrev_b32_e32 v68, 1, v68
	v_and_b32_e32 v121, 1, v147
	v_or_b32_e32 v68, v68, v121
	v_lshl_add_u32 v210, v68, 4, v120
	v_add_u32_e32 v211, 0x4800, v210
	v_xor_b32_e32 v68, 8, v68
	v_lshl_add_u32 v212, v68, 4, v120
	v_add_u32_e32 v212, 0x9000, v212
	v_add_u32_e32 v213, 0x4800, v212
	s_barrier
; #define LAS __attribute__((address_space(3)))
; __device__ __forceinline__ s16x4 lds_tr(lds_cptr p) { return __builtin_bit_cast(s16x4, __builtin_amdgcn_ds_read_tr16_b64_v4i16((LAS s16x4*)p)); }
;     ...
;     auto compute = [&]() __attribute__((always_inline)) {
; #pragma unroll
;         for (int kh = 0; kh < 2; ++kh) {
;             bf16x8 af[4], bfr[4];
; #pragma unroll
;             for (int m = 0; m < 4; ++m) af[m] = *(const LAS bf16x8*)(la + kh * GA_KH + m * 1024);
; #pragma unroll
;             for (int n = 0; n < 4; ++n) {
;                 const s16x4 r0 = lds_tr(lb + kh * 32 * GB_ST + n * 32), r1 = lds_tr(lb + kh * 32 * GB_ST + n * 32 + bsw);
;                 bfr[n] = (bf16x8){r0[0], r0[1], r0[2], r0[3], r1[0], r1[1], r1[2], r1[3]};
;             }
; #pragma unroll
;             for (int m = 0; m < 4; ++m)
; #pragma unroll
;                 for (int n = 0; n < 4; ++n) acc[m][n] = __builtin_amdgcn_mfma_f32_16x16x32_bf16(bfr[n], af[m], acc[m][n], 0, 0, 0);
;         }
;     };
;     ...
;     if (DEEP == 1) {
;         gloadA(0, ra0); gloadB(0, rb0); gloadA(1, ra1);
;         for (int kt = 0; kt < nk; kt += 2) {
;             __syncthreads();
;             lstore(ra0, rb0);
;             __syncthreads();
;             gloadB(kt + 1, rb0);
;             if (kt + 2 < nk) gloadA(kt + 2, ra0);
;             compute();
	s_add_u32 m0, s98, 0x0
	s_nop 0
	global_load_lds_dwordx4 v206, s[44:45]
	s_add_u32 m0, s98, 0x2040
	s_nop 0
	global_load_lds_dwordx4 v207, s[44:45]
	s_add_u32 m0, s98, 0x400
	s_nop 0
	global_load_lds_dwordx4 v208, s[44:45]
	s_add_u32 m0, s98, 0x2440
	s_nop 0
	global_load_lds_dwordx4 v209, s[44:45]
	s_add_u32 m0, s99, 0x4080
	s_nop 0
	global_load_lds_dwordx4 v210, s[46:47]
	s_add_u32 m0, s99, 0x4480
	s_nop 0
	global_load_lds_dwordx4 v211, s[46:47]
	s_add_u32 m0, s99, 0x4880
	s_nop 0
	global_load_lds_dwordx4 v212, s[46:47]
	s_add_u32 m0, s99, 0x4c80
	s_nop 0
	global_load_lds_dwordx4 v213, s[46:47]
	s_add_u32 s44, s44, 0x80
	s_addc_u32 s45, s45, 0
	s_add_u32 s46, s46, 0x48000
	s_addc_u32 s47, s47, 0
	v_mov_b32_e32 v21, v20
	v_mov_b32_e32 v22, v20
	v_mov_b32_e32 v23, v20
	v_mov_b32_e32 v32, v20
	v_mov_b32_e32 v33, v20
	v_mov_b32_e32 v34, v20
	v_mov_b32_e32 v35, v20
	v_mov_b32_e32 v4, v20
	v_mov_b32_e32 v5, v20
	v_mov_b32_e32 v6, v20
	v_mov_b32_e32 v7, v20
	v_mov_b32_e32 v8, v20
	v_mov_b32_e32 v9, v20
	v_mov_b32_e32 v10, v20
	v_mov_b32_e32 v11, v20
	v_mov_b32_e32 v12, v20
	v_mov_b32_e32 v13, v20
	v_mov_b32_e32 v14, v20
	v_mov_b32_e32 v15, v20
	v_mov_b32_e32 v16, v20
	v_mov_b32_e32 v17, v20
	v_mov_b32_e32 v18, v20
	v_mov_b32_e32 v19, v20
	v_mov_b32_e32 v24, v20
	v_mov_b32_e32 v25, v20
	v_mov_b32_e32 v26, v20
	v_mov_b32_e32 v27, v20
	v_mov_b32_e32 v28, v20
	v_mov_b32_e32 v29, v20
	v_mov_b32_e32 v30, v20
	v_mov_b32_e32 v31, v20
	v_mov_b32_e32 v36, v20
	v_mov_b32_e32 v37, v20
	v_mov_b32_e32 v38, v20
	v_mov_b32_e32 v39, v20
	v_mov_b32_e32 v40, v20
	v_mov_b32_e32 v41, v20
	v_mov_b32_e32 v42, v20
	v_mov_b32_e32 v43, v20
	v_mov_b32_e32 v44, v20
	v_mov_b32_e32 v45, v20
	v_mov_b32_e32 v46, v20
	v_mov_b32_e32 v47, v20
	v_mov_b32_e32 v48, v20
	v_mov_b32_e32 v49, v20
	v_mov_b32_e32 v50, v20
	v_mov_b32_e32 v51, v20
	v_mov_b32_e32 v52, v20
	v_mov_b32_e32 v53, v20
	v_mov_b32_e32 v54, v20
	v_mov_b32_e32 v55, v20
	v_mov_b32_e32 v56, v20
	v_mov_b32_e32 v57, v20
	v_mov_b32_e32 v58, v20
	v_mov_b32_e32 v59, v20
	v_mov_b32_e32 v60, v20
	v_mov_b32_e32 v61, v20
	v_mov_b32_e32 v62, v20
	v_mov_b32_e32 v63, v20
	v_mov_b32_e32 v64, v20
	v_mov_b32_e32 v65, v20
	v_mov_b32_e32 v66, v20
	v_mov_b32_e32 v67, v20
	s_waitcnt vmcnt(0)
	s_barrier
.Lip_loop:
	s_add_u32 m0, s98, 0x9000
	ds_read_b64_tr_b16 v[158:159], v214 offset:16512
	ds_read_b64_tr_b16 v[160:161], v214 offset:17536
	ds_read_b128 v[128:131], v216
	ds_read_b64_tr_b16 v[162:163], v215 offset:16512
	ds_read_b64_tr_b16 v[164:165], v215 offset:17536
	s_waitcnt lgkmcnt(2)
	v_mfma_f32_16x16x32_bf16 v[64:67], v[158:161], v[128:131], v[64:67]
	global_load_lds_dwordx4 v206, s[44:45]
	s_add_u32 m0, s98, 0xb040
	ds_read_b64_tr_b16 v[166:167], v217 offset:16512
	ds_read_b64_tr_b16 v[168:169], v217 offset:17536
	s_waitcnt lgkmcnt(2)
	v_mfma_f32_16x16x32_bf16 v[60:63], v[162:165], v[128:131], v[60:63]
	global_load_lds_dwordx4 v207, s[44:45]
	s_add_u32 m0, s98, 0x9400
	ds_read_b64_tr_b16 v[170:171], v218 offset:16512
	ds_read_b64_tr_b16 v[172:173], v218 offset:17536
	s_waitcnt lgkmcnt(2)
	v_mfma_f32_16x16x32_bf16 v[56:59], v[166:169], v[128:131], v[56:59]
	global_load_lds_dwordx4 v208, s[44:45]
	s_add_u32 m0, s98, 0xb440
	ds_read_b128 v[132:135], v216 offset:1024
	s_waitcnt lgkmcnt(1)
	v_mfma_f32_16x16x32_bf16 v[52:55], v[170:173], v[128:131], v[52:55]
	global_load_lds_dwordx4 v209, s[44:45]
	s_add_u32 m0, s99, 0xd080
	ds_read_b128 v[136:139], v216 offset:2048
	s_waitcnt lgkmcnt(1)
	v_mfma_f32_16x16x32_bf16 v[48:51], v[158:161], v[132:135], v[48:51]
	global_load_lds_dwordx4 v210, s[46:47]
	s_add_u32 m0, s99, 0xd480
	ds_read_b128 v[140:143], v216 offset:3072
	v_mfma_f32_16x16x32_bf16 v[44:47], v[162:165], v[132:135], v[44:47]
	global_load_lds_dwordx4 v211, s[46:47]
	s_add_u32 m0, s99, 0xd880
	ds_read_b64_tr_b16 v[174:175], v214 offset:24704
	ds_read_b64_tr_b16 v[176:177], v214 offset:25728
	v_mfma_f32_16x16x32_bf16 v[40:43], v[166:169], v[132:135], v[40:43]
	global_load_lds_dwordx4 v212, s[46:47]
	s_add_u32 m0, s99, 0xdc80
	ds_read_b64_tr_b16 v[178:179], v215 offset:24704
	ds_read_b64_tr_b16 v[180:181], v215 offset:25728
	v_mfma_f32_16x16x32_bf16 v[36:39], v[170:173], v[132:135], v[36:39]
	global_load_lds_dwordx4 v213, s[46:47]
	s_add_u32 s44, s44, 0x80
	s_addc_u32 s45, s45, 0
	s_add_u32 s46, s46, 0x48000
	s_addc_u32 s47, s47, 0
	ds_read_b128 v[128:131], v216 offset:8256
	s_waitcnt lgkmcnt(6)
	v_mfma_f32_16x16x32_bf16 v[28:31], v[158:161], v[136:139], v[28:31]
	ds_read_b64_tr_b16 v[182:183], v217 offset:24704
	ds_read_b64_tr_b16 v[184:185], v217 offset:25728
	v_mfma_f32_16x16x32_bf16 v[24:27], v[162:165], v[136:139], v[24:27]
	ds_read_b64_tr_b16 v[186:187], v218 offset:24704
	ds_read_b64_tr_b16 v[188:189], v218 offset:25728
	v_mfma_f32_16x16x32_bf16 v[16:19], v[166:169], v[136:139], v[16:19]
	v_mfma_f32_16x16x32_bf16 v[12:15], v[170:173], v[136:139], v[12:15]
	ds_read_b128 v[132:135], v216 offset:9280
	s_waitcnt lgkmcnt(10)
	v_mfma_f32_16x16x32_bf16 v[8:11], v[158:161], v[140:143], v[8:11]
	v_mfma_f32_16x16x32_bf16 v[4:7], v[162:165], v[140:143], v[4:7]
	v_mfma_f32_16x16x32_bf16 v[32:35], v[166:169], v[140:143], v[32:35]
	v_mfma_f32_16x16x32_bf16 v[20:23], v[170:173], v[140:143], v[20:23]
	ds_read_b128 v[136:139], v216 offset:10304
	s_waitcnt lgkmcnt(6)
	v_mfma_f32_16x16x32_bf16 v[64:67], v[174:177], v[128:131], v[64:67]
	v_mfma_f32_16x16x32_bf16 v[60:63], v[178:181], v[128:131], v[60:63]
	s_waitcnt lgkmcnt(4)
	v_mfma_f32_16x16x32_bf16 v[56:59], v[182:185], v[128:131], v[56:59]
	s_waitcnt lgkmcnt(2)
	v_mfma_f32_16x16x32_bf16 v[52:55], v[186:189], v[128:131], v[52:55]
	ds_read_b128 v[140:143], v216 offset:11328
	s_waitcnt lgkmcnt(2)
	v_mfma_f32_16x16x32_bf16 v[48:51], v[174:177], v[132:135], v[48:51]
	v_mfma_f32_16x16x32_bf16 v[44:47], v[178:181], v[132:135], v[44:47]
	v_mfma_f32_16x16x32_bf16 v[40:43], v[182:185], v[132:135], v[40:43]
	v_mfma_f32_16x16x32_bf16 v[36:39], v[186:189], v[132:135], v[36:39]
	s_waitcnt lgkmcnt(1)
	v_mfma_f32_16x16x32_bf16 v[28:31], v[174:177], v[136:139], v[28:31]
	v_mfma_f32_16x16x32_bf16 v[24:27], v[178:181], v[136:139], v[24:27]
	v_mfma_f32_16x16x32_bf16 v[16:19], v[182:185], v[136:139], v[16:19]
	v_mfma_f32_16x16x32_bf16 v[12:15], v[186:189], v[136:139], v[12:15]
	s_waitcnt lgkmcnt(0)
	v_mfma_f32_16x16x32_bf16 v[8:11], v[174:177], v[140:143], v[8:11]
	v_mfma_f32_16x16x32_bf16 v[4:7], v[178:181], v[140:143], v[4:7]
	v_mfma_f32_16x16x32_bf16 v[32:35], v[182:185], v[140:143], v[32:35]
	v_mfma_f32_16x16x32_bf16 v[20:23], v[186:189], v[140:143], v[20:23]
	s_waitcnt vmcnt(0) lgkmcnt(0)
	s_barrier
; #define LAS __attribute__((address_space(3)))
; __device__ __forceinline__ s16x4 lds_tr(lds_cptr p) { return __builtin_bit_cast(s16x4, __builtin_amdgcn_ds_read_tr16_b64_v4i16((LAS s16x4*)p)); }
;     ...
;     auto compute = [&]() __attribute__((always_inline)) {
; #pragma unroll
;         for (int kh = 0; kh < 2; ++kh) {
;             bf16x8 af[4], bfr[4];
; #pragma unroll
;             for (int m = 0; m < 4; ++m) af[m] = *(const LAS bf16x8*)(la + kh * GA_KH + m * 1024);
; #pragma unroll
;             for (int n = 0; n < 4; ++n) {
;                 const s16x4 r0 = lds_tr(lb + kh * 32 * GB_ST + n * 32), r1 = lds_tr(lb + kh * 32 * GB_ST + n * 32 + bsw);
;                 bfr[n] = (bf16x8){r0[0], r0[1], r0[2], r0[3], r1[0], r1[1], r1[2], r1[3]};
;             }
; #pragma unroll
;             for (int m = 0; m < 4; ++m)
; #pragma unroll
;                 for (int n = 0; n < 4; ++n) acc[m][n] = __builtin_amdgcn_mfma_f32_16x16x32_bf16(bfr[n], af[m], acc[m][n], 0, 0, 0);
;         }
;     };
;     ...
;             __syncthreads();
;             lstore(ra1, rb0);
;             __syncthreads();
;             if (kt + 2 < nk) gloadB(kt + 2, rb0);
;             if (kt + 3 < nk) gloadA(kt + 3, ra1);
;             compute();
;         }
;         return;
;     }
	s_add_u32 m0, s98, 0x0
	ds_read_b64_tr_b16 v[158:159], v214 offset:53376
	ds_read_b64_tr_b16 v[160:161], v214 offset:54400
	ds_read_b128 v[128:131], v216 offset:36864
	ds_read_b64_tr_b16 v[162:163], v215 offset:53376
	ds_read_b64_tr_b16 v[164:165], v215 offset:54400
	s_waitcnt lgkmcnt(2)
	v_mfma_f32_16x16x32_bf16 v[64:67], v[158:161], v[128:131], v[64:67]
	global_load_lds_dwordx4 v206, s[44:45]
	s_add_u32 m0, s98, 0x2040
	ds_read_b64_tr_b16 v[166:167], v217 offset:53376
	ds_read_b64_tr_b16 v[168:169], v217 offset:54400
	s_waitcnt lgkmcnt(2)
	v_mfma_f32_16x16x32_bf16 v[60:63], v[162:165], v[128:131], v[60:63]
	global_load_lds_dwordx4 v207, s[44:45]
	s_add_u32 m0, s98, 0x400
	ds_read_b64_tr_b16 v[170:171], v218 offset:53376
	ds_read_b64_tr_b16 v[172:173], v218 offset:54400
	s_waitcnt lgkmcnt(2)
	v_mfma_f32_16x16x32_bf16 v[56:59], v[166:169], v[128:131], v[56:59]
	global_load_lds_dwordx4 v208, s[44:45]
	s_add_u32 m0, s98, 0x2440
	ds_read_b128 v[132:135], v216 offset:37888
	s_waitcnt lgkmcnt(1)
	v_mfma_f32_16x16x32_bf16 v[52:55], v[170:173], v[128:131], v[52:55]
	global_load_lds_dwordx4 v209, s[44:45]
	s_add_u32 m0, s99, 0x4080
	ds_read_b128 v[136:139], v216 offset:38912
	s_waitcnt lgkmcnt(1)
	v_mfma_f32_16x16x32_bf16 v[48:51], v[158:161], v[132:135], v[48:51]
	global_load_lds_dwordx4 v210, s[46:47]
	s_add_u32 m0, s99, 0x4480
	ds_read_b128 v[140:143], v216 offset:39936
	v_mfma_f32_16x16x32_bf16 v[44:47], v[162:165], v[132:135], v[44:47]
	global_load_lds_dwordx4 v211, s[46:47]
	s_add_u32 m0, s99, 0x4880
	ds_read_b64_tr_b16 v[174:175], v214 offset:61568
	ds_read_b64_tr_b16 v[176:177], v214 offset:62592
	v_mfma_f32_16x16x32_bf16 v[40:43], v[166:169], v[132:135], v[40:43]
	global_load_lds_dwordx4 v212, s[46:47]
	s_add_u32 m0, s99, 0x4c80
	ds_read_b64_tr_b16 v[178:179], v215 offset:61568
	ds_read_b64_tr_b16 v[180:181], v215 offset:62592
	v_mfma_f32_16x16x32_bf16 v[36:39], v[170:173], v[132:135], v[36:39]
	global_load_lds_dwordx4 v213, s[46:47]
	s_add_u32 s44, s44, 0x80
	s_addc_u32 s45, s45, 0
	s_add_u32 s46, s46, 0x48000
	s_addc_u32 s47, s47, 0
	ds_read_b128 v[128:131], v216 offset:45120
	s_waitcnt lgkmcnt(6)
	v_mfma_f32_16x16x32_bf16 v[28:31], v[158:161], v[136:139], v[28:31]
	ds_read_b64_tr_b16 v[182:183], v217 offset:61568
	ds_read_b64_tr_b16 v[184:185], v217 offset:62592
	v_mfma_f32_16x16x32_bf16 v[24:27], v[162:165], v[136:139], v[24:27]
	ds_read_b64_tr_b16 v[186:187], v218 offset:61568
	ds_read_b64_tr_b16 v[188:189], v218 offset:62592
	v_mfma_f32_16x16x32_bf16 v[16:19], v[166:169], v[136:139], v[16:19]
	v_mfma_f32_16x16x32_bf16 v[12:15], v[170:173], v[136:139], v[12:15]
	ds_read_b128 v[132:135], v216 offset:46144
	s_waitcnt lgkmcnt(10)
	v_mfma_f32_16x16x32_bf16 v[8:11], v[158:161], v[140:143], v[8:11]
	v_mfma_f32_16x16x32_bf16 v[4:7], v[162:165], v[140:143], v[4:7]
	v_mfma_f32_16x16x32_bf16 v[32:35], v[166:169], v[140:143], v[32:35]
	v_mfma_f32_16x16x32_bf16 v[20:23], v[170:173], v[140:143], v[20:23]
	ds_read_b128 v[136:139], v216 offset:47168
	s_waitcnt lgkmcnt(6)
	v_mfma_f32_16x16x32_bf16 v[64:67], v[174:177], v[128:131], v[64:67]
	v_mfma_f32_16x16x32_bf16 v[60:63], v[178:181], v[128:131], v[60:63]
	s_waitcnt lgkmcnt(4)
	v_mfma_f32_16x16x32_bf16 v[56:59], v[182:185], v[128:131], v[56:59]
	s_waitcnt lgkmcnt(2)
	v_mfma_f32_16x16x32_bf16 v[52:55], v[186:189], v[128:131], v[52:55]
	ds_read_b128 v[140:143], v216 offset:48192
	s_waitcnt lgkmcnt(2)
	v_mfma_f32_16x16x32_bf16 v[48:51], v[174:177], v[132:135], v[48:51]
	v_mfma_f32_16x16x32_bf16 v[44:47], v[178:181], v[132:135], v[44:47]
	v_mfma_f32_16x16x32_bf16 v[40:43], v[182:185], v[132:135], v[40:43]
	v_mfma_f32_16x16x32_bf16 v[36:39], v[186:189], v[132:135], v[36:39]
	s_waitcnt lgkmcnt(1)
	v_mfma_f32_16x16x32_bf16 v[28:31], v[174:177], v[136:139], v[28:31]
	v_mfma_f32_16x16x32_bf16 v[24:27], v[178:181], v[136:139], v[24:27]
	v_mfma_f32_16x16x32_bf16 v[16:19], v[182:185], v[136:139], v[16:19]
	v_mfma_f32_16x16x32_bf16 v[12:15], v[186:189], v[136:139], v[12:15]
	s_waitcnt lgkmcnt(0)
	v_mfma_f32_16x16x32_bf16 v[8:11], v[174:177], v[140:143], v[8:11]
	v_mfma_f32_16x16x32_bf16 v[4:7], v[178:181], v[140:143], v[4:7]
	v_mfma_f32_16x16x32_bf16 v[32:35], v[182:185], v[140:143], v[32:35]
	v_mfma_f32_16x16x32_bf16 v[20:23], v[186:189], v[140:143], v[20:23]
	s_waitcnt vmcnt(0) lgkmcnt(0)
	s_barrier
	s_add_i32 s6, s6, 2
	s_cmp_lt_u32 s6, 14
	s_cbranch_scc1 .Lip_loop
; #define LAS __attribute__((address_space(3)))
; __device__ __forceinline__ s16x4 lds_tr(lds_cptr p) { return __builtin_bit_cast(s16x4, __builtin_amdgcn_ds_read_tr16_b64_v4i16((LAS s16x4*)p)); }
;     ...
;     auto compute = [&]() __attribute__((always_inline)) {
; #pragma unroll
;         for (int kh = 0; kh < 2; ++kh) {
;             bf16x8 af[4], bfr[4];
; #pragma unroll
;             for (int m = 0; m < 4; ++m) af[m] = *(const LAS bf16x8*)(la + kh * GA_KH + m * 1024);
; #pragma unroll
;             for (int n = 0; n < 4; ++n) {
;                 const s16x4 r0 = lds_tr(lb + kh * 32 * GB_ST + n * 32), r1 = lds_tr(lb + kh * 32 * GB_ST + n * 32 + bsw);
;                 bfr[n] = (bf16x8){r0[0], r0[1], r0[2], r0[3], r1[0], r1[1], r1[2], r1[3]};
;             }
; #pragma unroll
;             for (int m = 0; m < 4; ++m)
; #pragma unroll
;                 for (int n = 0; n < 4; ++n) acc[m][n] = __builtin_amdgcn_mfma_f32_16x16x32_bf16(bfr[n], af[m], acc[m][n], 0, 0, 0);
;         }
;     };
;     ...
;     if (DEEP == 1) {
;         gloadA(0, ra0); gloadB(0, rb0); gloadA(1, ra1);
;         for (int kt = 0; kt < nk; kt += 2) {
;             __syncthreads();
;             lstore(ra0, rb0);
;             __syncthreads();
;             gloadB(kt + 1, rb0);
;             if (kt + 2 < nk) gloadA(kt + 2, ra0);
;             compute();
	s_add_u32 m0, s98, 0x9000
	ds_read_b64_tr_b16 v[158:159], v214 offset:16512
	ds_read_b64_tr_b16 v[160:161], v214 offset:17536
	ds_read_b128 v[128:131], v216
	ds_read_b64_tr_b16 v[162:163], v215 offset:16512
	ds_read_b64_tr_b16 v[164:165], v215 offset:17536
	s_waitcnt lgkmcnt(2)
	v_mfma_f32_16x16x32_bf16 v[64:67], v[158:161], v[128:131], v[64:67]
	global_load_lds_dwordx4 v206, s[44:45]
	s_add_u32 m0, s98, 0xb040
	ds_read_b64_tr_b16 v[166:167], v217 offset:16512
	ds_read_b64_tr_b16 v[168:169], v217 offset:17536
	s_waitcnt lgkmcnt(2)
	v_mfma_f32_16x16x32_bf16 v[60:63], v[162:165], v[128:131], v[60:63]
	global_load_lds_dwordx4 v207, s[44:45]
	s_add_u32 m0, s98, 0x9400
	ds_read_b64_tr_b16 v[170:171], v218 offset:16512
	ds_read_b64_tr_b16 v[172:173], v218 offset:17536
	s_waitcnt lgkmcnt(2)
	v_mfma_f32_16x16x32_bf16 v[56:59], v[166:169], v[128:131], v[56:59]
	global_load_lds_dwordx4 v208, s[44:45]
	s_add_u32 m0, s98, 0xb440
	ds_read_b128 v[132:135], v216 offset:1024
	s_waitcnt lgkmcnt(1)
	v_mfma_f32_16x16x32_bf16 v[52:55], v[170:173], v[128:131], v[52:55]
	global_load_lds_dwordx4 v209, s[44:45]
	s_add_u32 m0, s99, 0xd080
	ds_read_b128 v[136:139], v216 offset:2048
	s_waitcnt lgkmcnt(1)
	v_mfma_f32_16x16x32_bf16 v[48:51], v[158:161], v[132:135], v[48:51]
	global_load_lds_dwordx4 v210, s[46:47]
	s_add_u32 m0, s99, 0xd480
	ds_read_b128 v[140:143], v216 offset:3072
	v_mfma_f32_16x16x32_bf16 v[44:47], v[162:165], v[132:135], v[44:47]
	global_load_lds_dwordx4 v211, s[46:47]
	s_add_u32 m0, s99, 0xd880
	ds_read_b64_tr_b16 v[174:175], v214 offset:24704
	ds_read_b64_tr_b16 v[176:177], v214 offset:25728
	v_mfma_f32_16x16x32_bf16 v[40:43], v[166:169], v[132:135], v[40:43]
	global_load_lds_dwordx4 v212, s[46:47]
	s_add_u32 m0, s99, 0xdc80
	ds_read_b64_tr_b16 v[178:179], v215 offset:24704
	ds_read_b64_tr_b16 v[180:181], v215 offset:25728
	v_mfma_f32_16x16x32_bf16 v[36:39], v[170:173], v[132:135], v[36:39]
	global_load_lds_dwordx4 v213, s[46:47]
	s_add_u32 s44, s44, 0x80
	s_addc_u32 s45, s45, 0
	s_add_u32 s46, s46, 0x48000
	s_addc_u32 s47, s47, 0
	ds_read_b128 v[128:131], v216 offset:8256
	s_waitcnt lgkmcnt(6)
	v_mfma_f32_16x16x32_bf16 v[28:31], v[158:161], v[136:139], v[28:31]
	ds_read_b64_tr_b16 v[182:183], v217 offset:24704
	ds_read_b64_tr_b16 v[184:185], v217 offset:25728
	v_mfma_f32_16x16x32_bf16 v[24:27], v[162:165], v[136:139], v[24:27]
	ds_read_b64_tr_b16 v[186:187], v218 offset:24704
	ds_read_b64_tr_b16 v[188:189], v218 offset:25728
	v_mfma_f32_16x16x32_bf16 v[16:19], v[166:169], v[136:139], v[16:19]
	v_mfma_f32_16x16x32_bf16 v[12:15], v[170:173], v[136:139], v[12:15]
	ds_read_b128 v[132:135], v216 offset:9280
	s_waitcnt lgkmcnt(10)
	v_mfma_f32_16x16x32_bf16 v[8:11], v[158:161], v[140:143], v[8:11]
	v_mfma_f32_16x16x32_bf16 v[4:7], v[162:165], v[140:143], v[4:7]
	v_mfma_f32_16x16x32_bf16 v[32:35], v[166:169], v[140:143], v[32:35]
	v_mfma_f32_16x16x32_bf16 v[20:23], v[170:173], v[140:143], v[20:23]
	ds_read_b128 v[136:139], v216 offset:10304
	s_waitcnt lgkmcnt(6)
	v_mfma_f32_16x16x32_bf16 v[64:67], v[174:177], v[128:131], v[64:67]
	v_mfma_f32_16x16x32_bf16 v[60:63], v[178:181], v[128:131], v[60:63]
	s_waitcnt lgkmcnt(4)
	v_mfma_f32_16x16x32_bf16 v[56:59], v[182:185], v[128:131], v[56:59]
	s_waitcnt lgkmcnt(2)
	v_mfma_f32_16x16x32_bf16 v[52:55], v[186:189], v[128:131], v[52:55]
	ds_read_b128 v[140:143], v216 offset:11328
	s_waitcnt lgkmcnt(2)
	v_mfma_f32_16x16x32_bf16 v[48:51], v[174:177], v[132:135], v[48:51]
	v_mfma_f32_16x16x32_bf16 v[44:47], v[178:181], v[132:135], v[44:47]
	v_mfma_f32_16x16x32_bf16 v[40:43], v[182:185], v[132:135], v[40:43]
	v_mfma_f32_16x16x32_bf16 v[36:39], v[186:189], v[132:135], v[36:39]
	s_waitcnt lgkmcnt(1)
	v_mfma_f32_16x16x32_bf16 v[28:31], v[174:177], v[136:139], v[28:31]
	v_mfma_f32_16x16x32_bf16 v[24:27], v[178:181], v[136:139], v[24:27]
	v_mfma_f32_16x16x32_bf16 v[16:19], v[182:185], v[136:139], v[16:19]
	v_mfma_f32_16x16x32_bf16 v[12:15], v[186:189], v[136:139], v[12:15]
	s_waitcnt lgkmcnt(0)
	v_mfma_f32_16x16x32_bf16 v[8:11], v[174:177], v[140:143], v[8:11]
	v_mfma_f32_16x16x32_bf16 v[4:7], v[178:181], v[140:143], v[4:7]
	v_mfma_f32_16x16x32_bf16 v[32:35], v[182:185], v[140:143], v[32:35]
	v_mfma_f32_16x16x32_bf16 v[20:23], v[186:189], v[140:143], v[20:23]
	s_waitcnt vmcnt(0) lgkmcnt(0)
	s_barrier
; #define LAS __attribute__((address_space(3)))
; __device__ __forceinline__ s16x4 lds_tr(lds_cptr p) { return __builtin_bit_cast(s16x4, __builtin_amdgcn_ds_read_tr16_b64_v4i16((LAS s16x4*)p)); }
;     ...
;     auto compute = [&]() __attribute__((always_inline)) {
; #pragma unroll
;         for (int kh = 0; kh < 2; ++kh) {
;             bf16x8 af[4], bfr[4];
; #pragma unroll
;             for (int m = 0; m < 4; ++m) af[m] = *(const LAS bf16x8*)(la + kh * GA_KH + m * 1024);
; #pragma unroll
;             for (int n = 0; n < 4; ++n) {
;                 const s16x4 r0 = lds_tr(lb + kh * 32 * GB_ST + n * 32), r1 = lds_tr(lb + kh * 32 * GB_ST + n * 32 + bsw);
;                 bfr[n] = (bf16x8){r0[0], r0[1], r0[2], r0[3], r1[0], r1[1], r1[2], r1[3]};
;             }
; #pragma unroll
;             for (int m = 0; m < 4; ++m)
; #pragma unroll
;                 for (int n = 0; n < 4; ++n) acc[m][n] = __builtin_amdgcn_mfma_f32_16x16x32_bf16(bfr[n], af[m], acc[m][n], 0, 0, 0);
;         }
;     };
	ds_read_b64_tr_b16 v[158:159], v214 offset:53376
	ds_read_b64_tr_b16 v[160:161], v214 offset:54400
	ds_read_b128 v[128:131], v216 offset:36864
	ds_read_b64_tr_b16 v[162:163], v215 offset:53376
	ds_read_b64_tr_b16 v[164:165], v215 offset:54400
	s_waitcnt lgkmcnt(2)
	v_mfma_f32_16x16x32_bf16 v[64:67], v[158:161], v[128:131], v[64:67]
	ds_read_b64_tr_b16 v[166:167], v217 offset:53376
	ds_read_b64_tr_b16 v[168:169], v217 offset:54400
	s_waitcnt lgkmcnt(2)
	v_mfma_f32_16x16x32_bf16 v[60:63], v[162:165], v[128:131], v[60:63]
	ds_read_b64_tr_b16 v[170:171], v218 offset:53376
	ds_read_b64_tr_b16 v[172:173], v218 offset:54400
	s_waitcnt lgkmcnt(2)
	v_mfma_f32_16x16x32_bf16 v[56:59], v[166:169], v[128:131], v[56:59]
	ds_read_b128 v[132:135], v216 offset:37888
	s_waitcnt lgkmcnt(1)
	v_mfma_f32_16x16x32_bf16 v[52:55], v[170:173], v[128:131], v[52:55]
	ds_read_b128 v[136:139], v216 offset:38912
	s_waitcnt lgkmcnt(1)
	v_mfma_f32_16x16x32_bf16 v[48:51], v[158:161], v[132:135], v[48:51]
	ds_read_b128 v[140:143], v216 offset:39936
	v_mfma_f32_16x16x32_bf16 v[44:47], v[162:165], v[132:135], v[44:47]
	ds_read_b64_tr_b16 v[174:175], v214 offset:61568
	ds_read_b64_tr_b16 v[176:177], v214 offset:62592
	v_mfma_f32_16x16x32_bf16 v[40:43], v[166:169], v[132:135], v[40:43]
	ds_read_b64_tr_b16 v[178:179], v215 offset:61568
	ds_read_b64_tr_b16 v[180:181], v215 offset:62592
	v_mfma_f32_16x16x32_bf16 v[36:39], v[170:173], v[132:135], v[36:39]
	ds_read_b128 v[128:131], v216 offset:45120
	s_waitcnt lgkmcnt(6)
	v_mfma_f32_16x16x32_bf16 v[28:31], v[158:161], v[136:139], v[28:31]
	ds_read_b64_tr_b16 v[182:183], v217 offset:61568
	ds_read_b64_tr_b16 v[184:185], v217 offset:62592
	v_mfma_f32_16x16x32_bf16 v[24:27], v[162:165], v[136:139], v[24:27]
	ds_read_b64_tr_b16 v[186:187], v218 offset:61568
	ds_read_b64_tr_b16 v[188:189], v218 offset:62592
	v_mfma_f32_16x16x32_bf16 v[16:19], v[166:169], v[136:139], v[16:19]
	v_mfma_f32_16x16x32_bf16 v[12:15], v[170:173], v[136:139], v[12:15]
	ds_read_b128 v[132:135], v216 offset:46144
	s_waitcnt lgkmcnt(10)
	v_mfma_f32_16x16x32_bf16 v[8:11], v[158:161], v[140:143], v[8:11]
	v_mfma_f32_16x16x32_bf16 v[4:7], v[162:165], v[140:143], v[4:7]
	v_mfma_f32_16x16x32_bf16 v[32:35], v[166:169], v[140:143], v[32:35]
	v_mfma_f32_16x16x32_bf16 v[20:23], v[170:173], v[140:143], v[20:23]
	ds_read_b128 v[136:139], v216 offset:47168
	s_waitcnt lgkmcnt(6)
	v_mfma_f32_16x16x32_bf16 v[64:67], v[174:177], v[128:131], v[64:67]
	v_mfma_f32_16x16x32_bf16 v[60:63], v[178:181], v[128:131], v[60:63]
	s_waitcnt lgkmcnt(4)
	v_mfma_f32_16x16x32_bf16 v[56:59], v[182:185], v[128:131], v[56:59]
	s_waitcnt lgkmcnt(2)
	v_mfma_f32_16x16x32_bf16 v[52:55], v[186:189], v[128:131], v[52:55]
	ds_read_b128 v[140:143], v216 offset:48192
	s_waitcnt lgkmcnt(2)
	v_mfma_f32_16x16x32_bf16 v[48:51], v[174:177], v[132:135], v[48:51]
	v_mfma_f32_16x16x32_bf16 v[44:47], v[178:181], v[132:135], v[44:47]
	v_mfma_f32_16x16x32_bf16 v[40:43], v[182:185], v[132:135], v[40:43]
	v_mfma_f32_16x16x32_bf16 v[36:39], v[186:189], v[132:135], v[36:39]
	s_waitcnt lgkmcnt(1)
	v_mfma_f32_16x16x32_bf16 v[28:31], v[174:177], v[136:139], v[28:31]
	v_mfma_f32_16x16x32_bf16 v[24:27], v[178:181], v[136:139], v[24:27]
	v_mfma_f32_16x16x32_bf16 v[16:19], v[182:185], v[136:139], v[16:19]
	v_mfma_f32_16x16x32_bf16 v[12:15], v[186:189], v[136:139], v[12:15]
	s_waitcnt lgkmcnt(0)
	v_mfma_f32_16x16x32_bf16 v[8:11], v[174:177], v[140:143], v[8:11]
	v_mfma_f32_16x16x32_bf16 v[4:7], v[178:181], v[140:143], v[4:7]
	v_mfma_f32_16x16x32_bf16 v[32:35], v[182:185], v[140:143], v[32:35]
	v_mfma_f32_16x16x32_bf16 v[20:23], v[186:189], v[140:143], v[20:23]
	s_waitcnt vmcnt(0) lgkmcnt(0)
	s_barrier
